# P5 selected-attention step loop: block ids + per-wave masks prefetched one step ahead into SGPRs (removes 4 serialized LDS round trips per step)
# speedup vs baseline: 1.0105x; 1.0105x over previous
; #define TA_ISSUE(n_) do { if (DRY == 2) break; const int _j = TA_BLK(n_); ta_issue(lds, (n_) & 3, Kbg + (size_t)_j * 64 * 128, Vbg + (size_t)_j * 8192, w, lane); } while (0)
;     ...
;         const int tq0 = t0 + 8 * w + (i >> 2), tq1 = tq0 + 4; const size_t tt0 = (size_t)b * S_ + tq0, tt1 = tt0 + 4; const int hh = g * 4 + (i & 3);
;         const QF q0 = load_qf(WSP(bf16_t, WS_QR) + tt0 * 1024 + hh * 128, g4), q1 = load_qf(WSP(bf16_t, WS_QR) + tt1 * 1024 + hh * 128, g4);
;         f32x4 O0[8], O1[8]; float l0 = 0.f, l1 = 0.f;
; #pragma unroll
;         for (int dt = 0; dt < 8; ++dt) { O0[dt] = (f32x4){0.f, 0.f, 0.f, 0.f}; O1[dt] = (f32x4){0.f, 0.f, 0.f, 0.f}; }
;         const bf16_t* Kbg = Kall + (size_t)bg * S_ * 128; const bf16_t* Vbg = VTall + (size_t)bg * 256 * 8192;
;     ...
;         if (MODE == MODE_SEL) {
;             TA_ISSUE(0); if (nblk > 1) TA_ISSUE(1);
;             for (int n = 0; n < nblk; n += 2) {
;                 asm volatile("s_waitcnt vmcnt(0)" ::: "memory"); __syncthreads();
;                 if (n + 2 < nblk) TA_ISSUE(n + 2);
;                 if (n + 3 < nblk) TA_ISSUE(n + 3);
;                 TA_DO(n);
;                 if (n + 1 < nblk) TA_DO(n + 1);
.LBB0_693:
	s_cmp_lt_i32 s74, 1
	s_cbranch_scc1 .LBB0_656
	v_mov_b32_e32 v4, v201
	v_mov_b32_e32 v5, v201
	v_mov_b32_e32 v2, v201
	v_mov_b32_e32 v3, v201
	v_mov_b32_e32 v62, 0
	v_mov_b64_e32 v[12:13], v[4:5]
	v_mov_b64_e32 v[20:21], v[4:5]
	v_mov_b64_e32 v[28:29], v[4:5]
	v_mov_b64_e32 v[36:37], v[4:5]
	v_mov_b64_e32 v[44:45], v[4:5]
	v_mov_b64_e32 v[52:53], v[4:5]
	v_mov_b64_e32 v[56:57], v[4:5]
	v_or_b32_e32 v227, 4, v226
	s_mov_b32 s77, 1
	v_add_u32_e32 v247, 1, v226
	v_add_u32_e32 v248, 2, v226
	s_mov_b32 s75, 0
	v_mov_b64_e32 v[10:11], v[2:3]
	v_mov_b64_e32 v[18:19], v[2:3]
	v_mov_b64_e32 v[26:27], v[2:3]
	v_mov_b64_e32 v[34:35], v[2:3]
	v_mov_b64_e32 v[42:43], v[2:3]
	v_mov_b64_e32 v[50:51], v[2:3]
	v_mov_b64_e32 v[54:55], v[2:3]
	v_mov_b32_e32 v63, v62
	v_mov_b32_e32 v64, v62
	v_mov_b32_e32 v65, v62
	v_mov_b32_e32 v58, v62
	v_mov_b32_e32 v59, v62
	v_mov_b32_e32 v60, v62
	v_mov_b32_e32 v61, v62
	v_mov_b32_e32 v46, v62
	v_mov_b32_e32 v47, v62
	v_mov_b32_e32 v48, v62
	v_mov_b32_e32 v49, v62
	v_mov_b32_e32 v38, v62
	v_mov_b32_e32 v39, v62
	v_mov_b32_e32 v40, v62
	v_mov_b32_e32 v41, v62
	v_mov_b32_e32 v30, v62
	v_mov_b32_e32 v31, v62
	v_mov_b32_e32 v32, v62
	v_mov_b32_e32 v33, v62
	v_mov_b32_e32 v22, v62
	v_mov_b32_e32 v23, v62
	v_mov_b32_e32 v24, v62
	v_mov_b32_e32 v25, v62
	v_mov_b32_e32 v14, v62
	v_mov_b32_e32 v15, v62
	v_mov_b32_e32 v16, v62
	v_mov_b32_e32 v17, v62
	v_mov_b32_e32 v6, v62
	v_mov_b32_e32 v7, v62
	v_mov_b32_e32 v8, v62
	v_mov_b32_e32 v9, v62
	v_mov_b32_e32 v224, v62
	v_mov_b32_e32 v225, v62
	v_mov_b32_e32 v249, s22
	ds_read_b128 v[250:253], v249
	s_waitcnt lgkmcnt(0)
	v_readfirstlane_b32 s86, v250
	v_readfirstlane_b32 s87, v251
	v_readfirstlane_b32 s84, v252
	v_readfirstlane_b32 s85, v253
	s_nop 3
	s_and_b32 s90, s86, 0xff
	s_lshl_b32 s90, s90, 5
	s_add_i32 s90, s90, s59
	s_and_b32 s91, s87, 0xff
	s_lshl_b32 s91, s91, 5
	s_add_i32 s91, s91, s59
	v_mov_b32_e32 v250, s90
	v_mov_b32_e32 v251, s91
	ds_read_b32 v250, v250
	ds_read_b32 v251, v251
	s_waitcnt lgkmcnt(0)
	v_readfirstlane_b32 s88, v250
	v_readfirstlane_b32 s89, v251
	s_nop 3
	s_waitcnt vmcnt(0)
.LBB0_695:
	s_waitcnt vmcnt(0)
	s_add_i32 s0, s77, 1
	s_cmp_ge_i32 s0, s74
	s_waitcnt lgkmcnt(0)
	s_barrier
	s_cbranch_scc1 .LBB0_697
	v_mov_b32_e32 v98, s84
	s_add_i32 s0, s75, 0x10000
	s_and_b32 s0, s0, 0x10000
	s_add_i32 s0, s0, 0
	s_add_i32 s1, s0, s55
	s_waitcnt lgkmcnt(0)
	v_ashrrev_i32_e32 v99, 31, v98
	v_lshlrev_b64 v[98:99], 14, v[98:99]
	v_lshl_add_u64 v[100:101], s[2:3], 0, v[98:99]
	v_lshl_add_u64 v[102:103], v[100:101], 0, v[202:203]
	v_lshl_add_u64 v[102:103], v[102:103], 0, v[200:201]
	s_mov_b32 m0, s1
	v_lshl_add_u64 v[100:101], v[100:101], 0, v[204:205]
	v_lshl_add_u64 v[98:99], s[48:49], 0, v[98:99]
	global_load_lds_dwordx4 v[102:103], off
	v_lshl_add_u64 v[100:101], v[100:101], 0, v[200:201]
	s_add_i32 m0, s0, s56
	v_mov_b32_e32 v215, v201
	global_load_lds_dwordx4 v[100:101], off
	v_lshl_add_u64 v[100:101], v[98:99], 0, v[206:207]
	v_lshl_add_u64 v[100:101], v[100:101], 0, v[214:215]
	s_add_i32 m0, s1, 0x4000
	v_lshl_add_u64 v[98:99], v[98:99], 0, v[208:209]
	v_mov_b32_e32 v217, v201
	s_add_i32 s0, s0, s57
	global_load_lds_dwordx4 v[100:101], off
	v_lshl_add_u64 v[98:99], v[98:99], 0, v[216:217]
	s_add_i32 m0, s0, 0x4000
	s_nop 0
	global_load_lds_dwordx4 v[98:99], off
.LBB0_697:
	s_add_i32 s76, s77, 2
	s_cmp_ge_i32 s76, s74
	s_cbranch_scc1 .LBB0_699
	v_mov_b32_e32 v98, s85
	s_add_i32 s0, s75, 0x18000
	s_and_b32 s0, s0, 0x18000
	s_add_i32 s0, s0, 0
	s_add_i32 s1, s0, s55
	s_waitcnt lgkmcnt(0)
	v_ashrrev_i32_e32 v99, 31, v98
	v_lshlrev_b64 v[98:99], 14, v[98:99]
	v_lshl_add_u64 v[100:101], s[2:3], 0, v[98:99]
	v_lshl_add_u64 v[102:103], v[100:101], 0, v[202:203]
	v_lshl_add_u64 v[102:103], v[102:103], 0, v[200:201]
	s_mov_b32 m0, s1
	v_lshl_add_u64 v[100:101], v[100:101], 0, v[204:205]
	v_lshl_add_u64 v[98:99], s[48:49], 0, v[98:99]
	global_load_lds_dwordx4 v[102:103], off
	v_lshl_add_u64 v[100:101], v[100:101], 0, v[200:201]
	s_add_i32 m0, s0, s56
	v_mov_b32_e32 v215, v201
	global_load_lds_dwordx4 v[100:101], off
	v_lshl_add_u64 v[100:101], v[98:99], 0, v[206:207]
	v_lshl_add_u64 v[100:101], v[100:101], 0, v[214:215]
	s_add_i32 m0, s1, 0x4000
	v_lshl_add_u64 v[98:99], v[98:99], 0, v[208:209]
	v_mov_b32_e32 v217, v201
	s_add_i32 s0, s0, s57
	global_load_lds_dwordx4 v[100:101], off
	v_lshl_add_u64 v[98:99], v[98:99], 0, v[216:217]
	s_add_i32 m0, s0, 0x4000
	s_nop 0
	global_load_lds_dwordx4 v[98:99], off
.LBB0_699:
	s_and_b32 s90, s84, 0xff
	s_lshl_b32 s90, s90, 5
	s_add_i32 s90, s90, s59
	s_and_b32 s91, s85, 0xff
	s_lshl_b32 s91, s91, 5
	s_add_i32 s91, s91, s59
	v_mov_b32_e32 v250, s90
	v_mov_b32_e32 v251, s91
	v_mov_b32_e32 v249, s22
	ds_read_b32 v250, v250
	ds_read_b32 v251, v251
	ds_read_b64 v[252:253], v249 offset:16
	v_mov_b32_e32 v215, s86
	s_and_b32 s0, s75, 0x10000
	s_mov_b32 s78, s88
	s_cmp_eq_u32 s78, 0
	s_cbranch_scc1 .LBB0_723
	s_add_i32 s14, s0, 0
	v_add_u32_e32 v122, s14, v233
	v_add_u32_e32 v130, v122, v234
	v_add_u32_e32 v131, v122, v235
	v_add_u32_e32 v132, v122, v236
	v_add_u32_e32 v133, v122, v237
	ds_read_b128 v[98:101], v130
	ds_read_b128 v[102:105], v130 offset:1024
	ds_read_b128 v[106:109], v131
	ds_read_b128 v[110:113], v131 offset:1024
	ds_read_b128 v[114:117], v132
	ds_read_b128 v[118:121], v132 offset:1024
	ds_read_b128 v[122:125], v133
	ds_read_b128 v[126:129], v133 offset:1024
	ds_read_b128 v[146:149], v130 offset:8192
	ds_read_b128 v[150:153], v130 offset:9216
	ds_read_b128 v[170:173], v131 offset:8192
	ds_read_b128 v[174:177], v131 offset:9216
	ds_read_b128 v[178:181], v132 offset:8192
	ds_read_b128 v[182:185], v132 offset:9216
	ds_read_b128 v[186:189], v133 offset:8192
	ds_read_b128 v[190:193], v133 offset:9216
	s_and_b32 s15, s78, 15
	s_cmp_lg_u32 s15, 0
	s_cselect_b64 s[0:1], -1, 0
	s_cmp_eq_u32 s15, 0
	s_cbranch_scc1 .LBB0_702
	s_waitcnt lgkmcnt(0)
	v_mfma_f32_16x16x32_bf16 v[130:133], v[98:101], v[66:69], 0
	v_mfma_f32_16x16x32_bf16 v[134:137], v[102:105], v[66:69], 0
	v_mfma_f32_16x16x32_bf16 v[130:133], v[106:109], v[70:73], v[130:133]
	v_mfma_f32_16x16x32_bf16 v[134:137], v[110:113], v[70:73], v[134:137]
	v_mfma_f32_16x16x32_bf16 v[130:133], v[114:117], v[74:77], v[130:133]
	v_mfma_f32_16x16x32_bf16 v[134:137], v[118:121], v[74:77], v[134:137]
	v_mfma_f32_16x16x32_bf16 v[162:165], v[122:125], v[78:81], v[130:133]
	v_mfma_f32_16x16x32_bf16 v[166:169], v[126:129], v[78:81], v[134:137]
	v_mfma_f32_16x16x32_bf16 v[130:133], v[146:149], v[66:69], 0
	v_mfma_f32_16x16x32_bf16 v[134:137], v[150:153], v[66:69], 0
	v_mfma_f32_16x16x32_bf16 v[130:133], v[170:173], v[70:73], v[130:133]
	v_mfma_f32_16x16x32_bf16 v[134:137], v[174:177], v[70:73], v[134:137]
	v_mfma_f32_16x16x32_bf16 v[130:133], v[178:181], v[74:77], v[130:133]
	v_mfma_f32_16x16x32_bf16 v[134:137], v[182:185], v[74:77], v[134:137]
	v_mfma_f32_16x16x32_bf16 v[154:157], v[186:189], v[78:81], v[130:133]
	v_mfma_f32_16x16x32_bf16 v[158:161], v[190:193], v[78:81], v[134:137]

; #define TA_ISSUE(n_) do { if (DRY == 2) break; const int _j = TA_BLK(n_); ta_issue(lds, (n_) & 3, Kbg + (size_t)_j * 64 * 128, Vbg + (size_t)_j * 8192, w, lane); } while (0)
;     ...
;         if (MODE == MODE_SEL) {
;             TA_ISSUE(0); if (nblk > 1) TA_ISSUE(1);
;             for (int n = 0; n < nblk; n += 2) {
;                 asm volatile("s_waitcnt vmcnt(0)" ::: "memory"); __syncthreads();
;                 if (n + 2 < nblk) TA_ISSUE(n + 2);
;                 if (n + 3 < nblk) TA_ISSUE(n + 3);
;                 TA_DO(n);
;                 if (n + 1 < nblk) TA_DO(n + 1);
.LBB0_722:
.LBB0_723:
	s_cmp_ge_i32 s77, s74
	s_cbranch_scc1 .LBB0_748
	s_waitcnt lgkmcnt(0)
	v_mov_b32_e32 v136, s87
	s_add_i32 s0, s75, 0x8000
	s_and_b32 s0, s0, 0x18000
	s_mov_b32 s77, s89
	s_cmp_eq_u32 s77, 0
	s_cbranch_scc1 .LBB0_748
	s_add_i32 s14, s0, 0
	v_add_u32_e32 v122, s14, v233
	v_add_u32_e32 v130, v122, v234
	v_add_u32_e32 v131, v122, v235
	v_add_u32_e32 v137, v122, v236
	v_add_u32_e32 v138, v122, v237
	ds_read_b128 v[98:101], v130
	ds_read_b128 v[102:105], v130 offset:1024
	ds_read_b128 v[106:109], v131
	ds_read_b128 v[110:113], v131 offset:1024
	ds_read_b128 v[114:117], v137
	ds_read_b128 v[118:121], v137 offset:1024
	ds_read_b128 v[122:125], v138
	ds_read_b128 v[126:129], v138 offset:1024
	ds_read_b128 v[132:135], v130 offset:8192
	ds_read_b128 v[150:153], v130 offset:9216
	ds_read_b128 v[170:173], v131 offset:8192
	ds_read_b128 v[174:177], v131 offset:9216
	ds_read_b128 v[178:181], v137 offset:8192
	ds_read_b128 v[182:185], v137 offset:9216
	ds_read_b128 v[186:189], v138 offset:8192
	ds_read_b128 v[190:193], v138 offset:9216
	s_and_b32 s15, s77, 15
	s_cmp_lg_u32 s15, 0
	s_cselect_b64 s[0:1], -1, 0
	s_cmp_eq_u32 s15, 0
	s_cbranch_scc1 .LBB0_727
	s_waitcnt lgkmcnt(0)
	v_mfma_f32_16x16x32_bf16 v[138:141], v[98:101], v[66:69], 0
	v_mfma_f32_16x16x32_bf16 v[142:145], v[102:105], v[66:69], 0
	v_mfma_f32_16x16x32_bf16 v[138:141], v[106:109], v[70:73], v[138:141]
	v_mfma_f32_16x16x32_bf16 v[142:145], v[110:113], v[70:73], v[142:145]
	v_mfma_f32_16x16x32_bf16 v[138:141], v[114:117], v[74:77], v[138:141]
	v_mfma_f32_16x16x32_bf16 v[142:145], v[118:121], v[74:77], v[142:145]
	v_mfma_f32_16x16x32_bf16 v[162:165], v[122:125], v[78:81], v[138:141]
	v_mfma_f32_16x16x32_bf16 v[166:169], v[126:129], v[78:81], v[142:145]
	v_mfma_f32_16x16x32_bf16 v[138:141], v[132:135], v[66:69], 0
	v_mfma_f32_16x16x32_bf16 v[142:145], v[150:153], v[66:69], 0
	v_mfma_f32_16x16x32_bf16 v[138:141], v[170:173], v[70:73], v[138:141]
	v_mfma_f32_16x16x32_bf16 v[142:145], v[174:177], v[70:73], v[142:145]
	v_mfma_f32_16x16x32_bf16 v[138:141], v[178:181], v[74:77], v[138:141]
	v_mfma_f32_16x16x32_bf16 v[142:145], v[182:185], v[74:77], v[142:145]
	v_mfma_f32_16x16x32_bf16 v[154:157], v[186:189], v[78:81], v[138:141]
	v_mfma_f32_16x16x32_bf16 v[158:161], v[190:193], v[78:81], v[142:145]

; #define TA_ISSUE(n_) do { if (DRY == 2) break; const int _j = TA_BLK(n_); ta_issue(lds, (n_) & 3, Kbg + (size_t)_j * 64 * 128, Vbg + (size_t)_j * 8192, w, lane); } while (0)
;     ...
;             TA_ISSUE(0); if (nblk > 1) TA_ISSUE(1);
;             for (int n = 0; n < nblk; n += 2) {
;                 asm volatile("s_waitcnt vmcnt(0)" ::: "memory"); __syncthreads();
;                 if (n + 2 < nblk) TA_ISSUE(n + 2);
;                 if (n + 3 < nblk) TA_ISSUE(n + 3);
;                 TA_DO(n);
;                 if (n + 1 < nblk) TA_DO(n + 1);
;             }
.LBB0_747:
.LBB0_748:
	s_waitcnt lgkmcnt(0)
	v_readfirstlane_b32 s88, v250
	v_readfirstlane_b32 s89, v251
	s_mov_b32 s86, s84
	s_mov_b32 s87, s85
	v_readfirstlane_b32 s84, v252
	v_readfirstlane_b32 s85, v253
	s_add_i32 s22, s22, 8
	s_add_i32 s75, s75, 0x10000
	s_add_i32 s0, s76, -1
	s_cmp_ge_i32 s0, s74
	s_cbranch_scc1 .LBB0_657
	s_mov_b32 s77, s76
	s_branch .LBB0_695
